# final + FILL_E 7 instead of 8
# baseline (speedup 1.0000x reference)
.LBB0_1641:
	s_mul_i32 s2, s76, 0xd760
	s_add_i32 s2, s2, 0xc300
	s_sub_i32 s82, s11, s4
	s_max_i32 s57, s50, s2
	s_mul_i32 s2, s82, 0x1c0
	s_add_i32 s2, s2, s57
	s_min_i32 s50, s2, 0x34920
	s_cmp_lt_i32 s74, 0
	s_mov_b64 s[2:3], -1
	s_cbranch_scc0 .LBB0_2087
	s_ashr_i32 s9, s10, 6
	s_not_b32 s83, s74
	s_lshl_b32 s3, s9, 3
	s_lshl_b32 s2, s83, 6
	s_add_i32 s54, s57, s3
	s_add_i32 s42, s54, s2
	s_cmp_lt_i32 s42, s50
	s_cselect_b32 s77, s42, -1
	s_cmp_lt_i32 s77, 0
	v_and_b32_e32 v132, 63, v1
	s_cbranch_scc1 .LBB0_1654
	s_mul_hi_u32 s2, s77, 0x9824d8ed
	s_lshr_b32 s2, s2, 15
	s_mul_i32 s3, s2, 0xd760
	s_sub_i32 s24, s77, s3
	s_cmpk_gt_u32 s24, 0xc2ff
	s_mov_b64 s[20:21], -1
	s_cbranch_scc0 .LBB0_1675
	s_add_i32 s20, s2, 1
	s_add_i32 s3, s24, 0xffff3d00
	s_cmpk_lt_u32 s3, 0x1400
	s_cselect_b32 s3, s3, s24
	s_cmpk_gt_u32 s3, 0xbff
	s_mov_b64 s[22:23], -1
	s_cbranch_scc0 .LBB0_1672
	s_cmpk_gt_u32 s3, 0x13ff
	s_cbranch_scc0 .LBB0_1669
	s_add_u32 s25, s78, 0x6200000
	s_addc_u32 s26, s79, 0
	s_cmpk_gt_u32 s3, 0x93ff
	s_cbranch_scc0 .LBB0_1666
	s_add_u32 s27, s78, 0x26a00000
	s_addc_u32 s28, s79, 0
	s_cmpk_gt_u32 s3, 0xd3ff
	s_cbranch_scc0 .LBB0_1663
	s_cmpk_gt_u32 s3, 0xd5ff
	s_cbranch_scc0 .LBB0_1660
	s_cmpk_gt_u32 s3, 0xd6ff
	s_cbranch_scc0 .LBB0_1657
	s_lshl_b32 s22, s3, 5
	s_cmpk_gt_u32 s3, 0xd71f
	s_mov_b64 s[18:19], -1
	s_cbranch_scc0 .LBB0_1652
	s_mov_b32 s21, s47
	v_readlane_b32 s56, v243, 40
	s_lshl_b64 s[10:11], s[20:21], 19
	v_readlane_b32 s62, v243, 46
	v_readlane_b32 s63, v243, 47
	s_add_u32 s16, s62, s10
	s_addc_u32 s17, s63, s11
	s_lshl_b64 s[10:11], s[20:21], 18
	s_add_u32 s8, s78, s10
	s_addc_u32 s13, s79, s11
	s_add_u32 s10, s8, 0x37000000
	s_addc_u32 s11, s13, 0
	s_add_u32 s12, s8, 0x37100000
	v_readlane_b32 s58, v243, 42
	s_addc_u32 s13, s13, 0
	s_lshl_b32 s8, s20, 13
	v_readlane_b32 s59, v243, 43
	s_add_u32 s14, s58, s8
	s_addc_u32 s15, s59, 0
	s_and_b32 s8, s22, 0x7fffffc0
	v_readlane_b32 s57, v243, 41
	v_readlane_b32 s60, v243, 44
	v_readlane_b32 s61, v243, 45
	v_readlane_b32 s64, v243, 48
	v_readlane_b32 s65, v243, 49
	v_readlane_b32 s66, v243, 50
	v_readlane_b32 s67, v243, 51
	v_readlane_b32 s68, v243, 52
	v_readlane_b32 s69, v243, 53
	v_readlane_b32 s70, v243, 54
	v_readlane_b32 s71, v243, 55
	s_add_i32 s8, s8, 0xffe51c00
	s_and_b32 s89, s22, 32
	s_mov_b64 s[18:19], 0
